# code placement: P8 K-loop +12 bytes and P9 K-loop +44 bytes, chosen so that every M-segment's opening s_barrier and its first MFMA sit in the same 64-byte line
# speedup vs baseline: 1.0020x; 1.0020x over previous
.LBB0_1167:
	s_nop 0
	s_nop 0
	s_nop 0
	v_readlane_b32 s2, v251, 14
	v_readlane_b32 s3, v251, 15
	s_cmp_lt_i32 s2, 9
	s_cselect_b64 s[2:3], -1, 0
	s_and_b64 s[0:1], s[2:3], s[0:1]
	s_andn2_b64 vcc, exec, s[0:1]
	s_cbranch_vccnz .LBB0_1200
	v_readlane_b32 s0, v251, 16
	v_mbcnt_lo_u32_b32 v0, -1, 0
	v_mbcnt_hi_u32_b32 v0, -1, v0
	s_andn2_b32 s0, s0, 63
	s_nop 0
	v_add_u32_e32 v0, s0, v0
	v_cmp_gt_i32_e32 vcc, 33, v0
	s_waitcnt lgkmcnt(0)
	v_lshl_add_u32 v2, v0, 2, 0
	s_and_saveexec_b64 s[4:5], vcc
	s_cbranch_execz .LBB0_1170
	v_readlane_b32 s8, v251, 10
	v_ashrrev_i32_e32 v1, 31, v0
	v_readlane_b32 s10, v251, 12
	v_readlane_b32 s11, v251, 13
	v_add_u32_e32 v3, 0x24240, v2
	v_readlane_b32 s9, v251, 11
	v_lshl_add_u64 v[4:5], v[0:1], 2, s[10:11]
	v_add_co_u32_e32 v4, vcc, 0x66280000, v4
	s_nop 1
	v_addc_co_u32_e32 v5, vcc, 0, v5, vcc
	global_load_dword v1, v[4:5], off
	s_waitcnt vmcnt(0)
	ds_write_b32 v3, v1
